# speedup vs baseline: 1.0030x; 1.0030x over previous
.LBB3_33:
	s_waitcnt lgkmcnt(0)
	s_barrier
	s_add_i32 s60, s45, 16
	s_and_b32 s60, s60, 28
	s_or_b32 s60, s60, 2
	s_lshl_b32 s60, s60, 15
	s_or_b32 s61, s60, 0x4000
	s_mov_b32 m0, s38
	s_nop 0
	buffer_load_dwordx4 v166, s[12:15], s61 offen lds
	s_or_b32 s61, s60, 0x6000
	s_mov_b32 m0, s39
	s_nop 0
	buffer_load_dwordx4 v166, s[12:15], s61 offen lds
	s_or_b32 s61, s60, 0xc000
	s_mov_b32 m0, s40
	s_nop 0
	buffer_load_dwordx4 v166, s[12:15], s61 offen lds
	s_or_b32 s61, s60, 0xe000
	s_mov_b32 m0, s42
	s_nop 0
	buffer_load_dwordx4 v166, s[12:15], s61 offen lds
	s_lshr_b32 s62, s21, 1
	s_lshr_b32 s63, s20, 2
	s_xor_b32 s62, s62, s63
	s_and_b32 s62, s62, 1
	s_lshl_b32 s63, s62, 16
	v_add_u32_e32 v232, s63, v168
	v_add_u32_e32 v233, 0x8000, v232
	s_add_i32 s63, s45, 16
	s_and_b32 s63, s63, 28
	s_lshl_b32 s64, s62, 1
	s_or_b32 s63, s63, s64
	s_add_i32 s63, s63, s41
	s_lshl_b32 s63, s63, 1
	v_mov_b32_e32 v234, s63
	s_or_b32 s63, s63, 1
	v_mov_b32_e32 v235, s63
	s_lshl_b32 s64, s62, 8
	s_add_i32 s64, s64, s47
	s_add_i32 s64, s64, 0x20600
	v_lshl_add_u32 v236, v167, 2, s64
	s_waitcnt vmcnt(4)
	s_barrier
	v_mbcnt_lo_u32_b32 v185, -1, 0
	v_mbcnt_hi_u32_b32 v185, -1, v185
	s_lshl_b32 s69, s21, 5
	s_lshl_b64 s[76:77], s[16:17], 13
	s_add_u32 s76, s10, s76
	s_addc_u32 s77, s11, s77
	s_movk_i32 s72, 0xff80
	s_brev_b32 s73, -2
	v_add_u32_e32 v186, s69, v185
	v_cmp_gt_u32_e32 vcc, 32, v185
	s_and_saveexec_b64 s[70:71], vcc
	v_mov_b32_e32 v188, 0x20000
	v_lshl_add_u32 v188, v186, 2, v188
	ds_read_b32 v188, v188
	s_movk_i32 s74, 0x63
	v_and_b32_e32 v190, 0x7f, v186
	s_waitcnt lgkmcnt(0)
	v_ashrrev_i32_e32 v189, 31, v188
	v_and_b32_e32 v191, 0x7fffffff, v189
	v_bitop3_b32 v189, v189, v188, s73 bitop3:0x6c
	v_lshlrev_b32_e32 v192, 2, v189
	v_and_b32_e32 v192, 16, v192
	s_lshl_b32 s73, s20, 7
	v_bitop3_b32 v191, v191, s74, v188 bitop3:0x48
	v_or3_b32 v191, v191, s73, v192
	v_bfrev_b32_e32 v192, 1
	v_cmp_lt_i32_e32 vcc, -1, v188
	v_lshrrev_b32_e32 v193, 1, v189
	v_and_b32_e32 v193, 12, v193
	v_cndmask_b32_e32 v188, -1, v192, vcc
	v_bitop3_b32 v189, v189, v188, s72 bitop3:0x6c
	s_movk_i32 s72, 0x3ff
	v_bitop3_b32 v188, v191, s72, v193 bitop3:0x36
	s_lshl_b32 s72, s22, 7
	s_addk_i32 s72, 0x80
	v_add_u32_e32 v186, s72, v186
	s_movk_i32 s72, 0x380
	v_and_or_b32 v186, v186, s72, v190
	v_lshlrev_b32_e32 v186, 3, v186
	global_atomic_umax_x2 v186, v[188:189], s[76:77]
	s_or_b64 exec, exec, s[70:71]
	s_movk_i32 s65, 0xffc0
	s_movk_i32 s66, 0xff80
	s_brev_b32 s67, -2
	s_add_i32 s68, s45, 12
	s_and_b32 s68, s68, 28
	s_or_b32 s68, s68, 2
	s_add_i32 s68, s68, s41
	s_lshl_b32 s68, s68, 1
	v_mov_b32_e32 v176, s68
	s_or_b32 s68, s68, 1
	v_mov_b32_e32 v177, s68
	s_add_i32 s68, s47, 0x20500
	v_lshl_add_u32 v182, v167, 2, s68
	ds_read_b128 v[144:147], v232 offset:0
	ds_read_b128 v[148:151], v232 offset:256
	ds_read_b128 v[152:155], v232 offset:2048
	ds_read_b128 v[156:159], v232 offset:2304
	ds_read_b128 v[224:227], v232 offset:4096
	s_waitcnt lgkmcnt(4)
	v_mfma_f32_16x16x32_bf16 v[208:211], v[0:3], v[144:147], 0
	v_mfma_f32_16x16x32_bf16 v[212:215], v[4:7], v[144:147], 0
	ds_read_b128 v[228:231], v232 offset:4352
	s_waitcnt lgkmcnt(4)
	v_mfma_f32_16x16x32_bf16 v[216:219], v[0:3], v[148:151], 0
	v_mfma_f32_16x16x32_bf16 v[220:223], v[4:7], v[148:151], 0
	ds_read_b128 v[144:147], v232 offset:6144
	s_waitcnt lgkmcnt(4)
	v_mfma_f32_16x16x32_bf16 v[208:211], v[8:11], v[152:155], v[208:211]
	v_mfma_f32_16x16x32_bf16 v[212:215], v[12:15], v[152:155], v[212:215]
	ds_read_b128 v[148:151], v232 offset:6400
	v_and_or_b32 v180, v136, s65, v176
	v_and_or_b32 v181, v140, s65, v177
	v_max3_f32 v161, v161, v180, v181
	v_and_b32_e32 v178, 0xffffff80, v136
	v_and_b32_e32 v179, 0xffffff80, v140
	s_waitcnt lgkmcnt(4)
	v_mfma_f32_16x16x32_bf16 v[216:219], v[8:11], v[156:159], v[216:219]
	v_mfma_f32_16x16x32_bf16 v[220:223], v[12:15], v[156:159], v[220:223]
	ds_read_b128 v[152:155], v232 offset:8192
	v_and_or_b32 v180, v137, s65, v176
	v_and_or_b32 v181, v141, s65, v177
	v_max3_f32 v160, v160, v180, v181
	v_and_or_b32 v180, v137, s66, 1
	v_and_or_b32 v181, v141, s66, 1
	v_max_f32_e32 v178, v178, v180
	v_max_f32_e32 v179, v179, v181
	s_waitcnt lgkmcnt(4)
	v_mfma_f32_16x16x32_bf16 v[208:211], v[16:19], v[224:227], v[208:211]
	v_mfma_f32_16x16x32_bf16 v[212:215], v[20:23], v[224:227], v[212:215]
	ds_read_b128 v[156:159], v232 offset:8448
	v_and_or_b32 v180, v138, s65, v176
	v_and_or_b32 v181, v142, s65, v177
	v_max3_f32 v162, v162, v180, v181
	v_and_or_b32 v180, v138, s66, 2
	v_and_or_b32 v181, v142, s66, 2
	v_max_f32_e32 v178, v178, v180
	v_max_f32_e32 v179, v179, v181
	s_waitcnt lgkmcnt(4)
	v_mfma_f32_16x16x32_bf16 v[216:219], v[16:19], v[228:231], v[216:219]
	v_mfma_f32_16x16x32_bf16 v[220:223], v[20:23], v[228:231], v[220:223]
	ds_read_b128 v[224:227], v232 offset:10240
	v_and_or_b32 v180, v139, s65, v176
	v_and_or_b32 v181, v143, s65, v177
	v_max3_f32 v163, v163, v180, v181
	v_and_or_b32 v180, v139, s66, 3
	v_and_or_b32 v181, v143, s66, 3
	v_max_f32_e32 v178, v178, v180
	v_max_f32_e32 v179, v179, v181
	s_waitcnt lgkmcnt(4)
	v_mfma_f32_16x16x32_bf16 v[208:211], v[24:27], v[144:147], v[208:211]
	v_mfma_f32_16x16x32_bf16 v[212:215], v[28:31], v[144:147], v[212:215]
	ds_read_b128 v[228:231], v232 offset:10496
	v_and_or_b32 v180, v128, s65, v176
	v_and_or_b32 v181, v132, s65, v177
	v_max3_f32 v203, v203, v180, v181
	v_and_or_b32 v180, v128, s66, 4
	v_and_or_b32 v181, v132, s66, 4
	v_max_f32_e32 v178, v178, v180
	v_max_f32_e32 v179, v179, v181
	s_waitcnt lgkmcnt(4)
	v_mfma_f32_16x16x32_bf16 v[216:219], v[24:27], v[148:151], v[216:219]
	v_mfma_f32_16x16x32_bf16 v[220:223], v[28:31], v[148:151], v[220:223]
	ds_read_b128 v[144:147], v232 offset:12288
	v_and_or_b32 v180, v129, s65, v176
	v_and_or_b32 v181, v133, s65, v177
	v_max3_f32 v204, v204, v180, v181
	v_and_or_b32 v180, v129, s66, 5
	v_and_or_b32 v181, v133, s66, 5
	v_max_f32_e32 v178, v178, v180
	v_max_f32_e32 v179, v179, v181
	s_waitcnt lgkmcnt(4)
	v_mfma_f32_16x16x32_bf16 v[208:211], v[32:35], v[152:155], v[208:211]
	v_mfma_f32_16x16x32_bf16 v[212:215], v[36:39], v[152:155], v[212:215]
	ds_read_b128 v[148:151], v232 offset:12544
	v_and_or_b32 v180, v130, s65, v176
	v_and_or_b32 v181, v134, s65, v177
	v_max3_f32 v205, v205, v180, v181
	v_and_or_b32 v180, v130, s66, 6
	v_and_or_b32 v181, v134, s66, 6
	v_max_f32_e32 v178, v178, v180
	v_max_f32_e32 v179, v179, v181
	s_waitcnt lgkmcnt(4)
	v_mfma_f32_16x16x32_bf16 v[216:219], v[32:35], v[156:159], v[216:219]
	v_mfma_f32_16x16x32_bf16 v[220:223], v[36:39], v[156:159], v[220:223]
	ds_read_b128 v[152:155], v232 offset:14336
	v_and_or_b32 v180, v131, s65, v176
	v_and_or_b32 v181, v135, s65, v177
	v_max3_f32 v206, v206, v180, v181
	v_and_or_b32 v180, v131, s66, 7
	v_and_or_b32 v181, v135, s66, 7
	v_max_f32_e32 v178, v178, v180
	v_max_f32_e32 v179, v179, v181
	s_waitcnt lgkmcnt(4)
	v_mfma_f32_16x16x32_bf16 v[208:211], v[40:43], v[224:227], v[208:211]
	v_mfma_f32_16x16x32_bf16 v[212:215], v[44:47], v[224:227], v[212:215]
	ds_read_b128 v[156:159], v232 offset:14592
	v_or_b32_e32 v183, v173, v178
	v_ashrrev_i32_e32 v180, 31, v178
	v_bitop3_b32 v183, v180, v183, s67 bitop3:0x6c
	v_or_b32_e32 v184, v173, v179
	v_ashrrev_i32_e32 v181, 31, v179
	v_bitop3_b32 v184, v181, v184, s67 bitop3:0x6c
	s_waitcnt lgkmcnt(4)
	v_mfma_f32_16x16x32_bf16 v[216:219], v[40:43], v[228:231], v[216:219]
	v_mfma_f32_16x16x32_bf16 v[220:223], v[44:47], v[228:231], v[220:223]
	s_waitcnt lgkmcnt(3)
	v_mfma_f32_16x16x32_bf16 v[208:211], v[48:51], v[144:147], v[208:211]
	v_mfma_f32_16x16x32_bf16 v[212:215], v[52:55], v[144:147], v[212:215]
	s_waitcnt lgkmcnt(2)
	v_mfma_f32_16x16x32_bf16 v[216:219], v[48:51], v[148:151], v[216:219]
	v_mfma_f32_16x16x32_bf16 v[220:223], v[52:55], v[148:151], v[220:223]
	s_waitcnt lgkmcnt(1)
	v_mfma_f32_16x16x32_bf16 v[208:211], v[56:59], v[152:155], v[208:211]
	v_mfma_f32_16x16x32_bf16 v[212:215], v[60:63], v[152:155], v[212:215]
	s_waitcnt lgkmcnt(0)
	v_mfma_f32_16x16x32_bf16 v[216:219], v[56:59], v[156:159], v[216:219]
	v_mfma_f32_16x16x32_bf16 v[220:223], v[60:63], v[156:159], v[220:223]
	s_waitcnt vmcnt(1)
	s_barrier
	ds_read_b128 v[144:147], v233 offset:0
	ds_read_b128 v[148:151], v233 offset:256
	ds_read_b128 v[152:155], v233 offset:2048
	ds_read_b128 v[156:159], v233 offset:2304
	ds_read_b128 v[224:227], v233 offset:4096
	s_waitcnt lgkmcnt(4)
	v_mfma_f32_16x16x32_bf16 v[208:211], v[64:67], v[144:147], v[208:211]
	v_mfma_f32_16x16x32_bf16 v[212:215], v[68:71], v[144:147], v[212:215]
	ds_read_b128 v[228:231], v233 offset:4352
	s_waitcnt lgkmcnt(4)
	v_mfma_f32_16x16x32_bf16 v[216:219], v[64:67], v[148:151], v[216:219]
	v_mfma_f32_16x16x32_bf16 v[220:223], v[68:71], v[148:151], v[220:223]
	ds_read_b128 v[144:147], v233 offset:6144
	s_waitcnt lgkmcnt(4)
	v_mfma_f32_16x16x32_bf16 v[208:211], v[72:75], v[152:155], v[208:211]
	v_mfma_f32_16x16x32_bf16 v[212:215], v[76:79], v[152:155], v[212:215]
	ds_read_b128 v[148:151], v233 offset:6400
	s_waitcnt lgkmcnt(4)
	v_mfma_f32_16x16x32_bf16 v[216:219], v[72:75], v[156:159], v[216:219]
	v_mfma_f32_16x16x32_bf16 v[220:223], v[76:79], v[156:159], v[220:223]
	ds_read_b128 v[152:155], v233 offset:8192
	s_waitcnt lgkmcnt(4)
	v_mfma_f32_16x16x32_bf16 v[208:211], v[80:83], v[224:227], v[208:211]
	v_mfma_f32_16x16x32_bf16 v[212:215], v[84:87], v[224:227], v[212:215]
	ds_read_b128 v[156:159], v233 offset:8448
	s_waitcnt lgkmcnt(4)
	v_mfma_f32_16x16x32_bf16 v[216:219], v[80:83], v[228:231], v[216:219]
	v_mfma_f32_16x16x32_bf16 v[220:223], v[84:87], v[228:231], v[220:223]
	ds_read_b128 v[224:227], v233 offset:10240
	s_waitcnt lgkmcnt(4)
	v_mfma_f32_16x16x32_bf16 v[208:211], v[88:91], v[144:147], v[208:211]
	v_mfma_f32_16x16x32_bf16 v[212:215], v[92:95], v[144:147], v[212:215]
	ds_read_b128 v[228:231], v233 offset:10496
	s_waitcnt lgkmcnt(4)
	v_mfma_f32_16x16x32_bf16 v[216:219], v[88:91], v[148:151], v[216:219]
	v_mfma_f32_16x16x32_bf16 v[220:223], v[92:95], v[148:151], v[220:223]
	ds_read_b128 v[144:147], v233 offset:12288
	s_waitcnt lgkmcnt(4)
	v_mfma_f32_16x16x32_bf16 v[208:211], v[96:99], v[152:155], v[208:211]
	v_mfma_f32_16x16x32_bf16 v[212:215], v[100:103], v[152:155], v[212:215]
	ds_read_b128 v[148:151], v233 offset:12544
	s_waitcnt lgkmcnt(4)
	v_mfma_f32_16x16x32_bf16 v[216:219], v[96:99], v[156:159], v[216:219]
	v_mfma_f32_16x16x32_bf16 v[220:223], v[100:103], v[156:159], v[220:223]
	ds_read_b128 v[152:155], v233 offset:14336
	s_waitcnt lgkmcnt(4)
	v_mfma_f32_16x16x32_bf16 v[208:211], v[104:107], v[224:227], v[208:211]
	v_mfma_f32_16x16x32_bf16 v[212:215], v[108:111], v[224:227], v[212:215]
	ds_read_b128 v[156:159], v233 offset:14592
	s_waitcnt lgkmcnt(4)
	v_mfma_f32_16x16x32_bf16 v[216:219], v[104:107], v[228:231], v[216:219]
	v_mfma_f32_16x16x32_bf16 v[220:223], v[108:111], v[228:231], v[220:223]
	s_waitcnt lgkmcnt(3)
	v_mfma_f32_16x16x32_bf16 v[208:211], v[112:115], v[144:147], v[208:211]
	v_mfma_f32_16x16x32_bf16 v[212:215], v[116:119], v[144:147], v[212:215]
	s_waitcnt lgkmcnt(2)
	v_mfma_f32_16x16x32_bf16 v[216:219], v[112:115], v[148:151], v[216:219]
	v_mfma_f32_16x16x32_bf16 v[220:223], v[116:119], v[148:151], v[220:223]
	s_waitcnt lgkmcnt(1)
	v_mfma_f32_16x16x32_bf16 v[208:211], v[120:123], v[152:155], v[208:211]
	v_mfma_f32_16x16x32_bf16 v[212:215], v[124:127], v[152:155], v[212:215]
	s_waitcnt lgkmcnt(0)
	v_mfma_f32_16x16x32_bf16 v[216:219], v[120:123], v[156:159], v[216:219]
	v_mfma_f32_16x16x32_bf16 v[220:223], v[124:127], v[156:159], v[220:223]
	s_nop 7
	s_nop 3
	v_and_or_b32 v237, v208, s65, v234
	v_and_or_b32 v238, v216, s65, v235
	v_max3_f32 v161, v161, v237, v238
	v_and_b32_e32 v174, 0xffffff80, v208
	v_and_b32_e32 v175, 0xffffff80, v216
	v_and_or_b32 v237, v209, s65, v234
	v_and_or_b32 v238, v217, s65, v235
	v_max3_f32 v160, v160, v237, v238
	v_and_or_b32 v237, v209, s66, 1
	v_and_or_b32 v238, v217, s66, 1
	v_max_f32_e32 v174, v174, v237
	v_max_f32_e32 v175, v175, v238
	v_and_or_b32 v237, v210, s65, v234
	v_and_or_b32 v238, v218, s65, v235
	v_max3_f32 v162, v162, v237, v238
	v_and_or_b32 v237, v210, s66, 2
	v_and_or_b32 v238, v218, s66, 2
	v_max_f32_e32 v174, v174, v237
	v_max_f32_e32 v175, v175, v238
	v_and_or_b32 v237, v211, s65, v234
	v_and_or_b32 v238, v219, s65, v235
	v_max3_f32 v163, v163, v237, v238
	v_and_or_b32 v237, v211, s66, 3
	v_and_or_b32 v238, v219, s66, 3
	v_max_f32_e32 v174, v174, v237
	v_max_f32_e32 v175, v175, v238
	v_and_or_b32 v237, v212, s65, v234
	v_and_or_b32 v238, v220, s65, v235
	v_max3_f32 v203, v203, v237, v238
	v_and_or_b32 v237, v212, s66, 4
	v_and_or_b32 v238, v220, s66, 4
	v_max_f32_e32 v174, v174, v237
	v_max_f32_e32 v175, v175, v238
	v_and_or_b32 v237, v213, s65, v234
	v_and_or_b32 v238, v221, s65, v235
	v_max3_f32 v204, v204, v237, v238
	v_and_or_b32 v237, v213, s66, 5
	v_and_or_b32 v238, v221, s66, 5
	v_max_f32_e32 v174, v174, v237
	v_max_f32_e32 v175, v175, v238
	v_and_or_b32 v237, v214, s65, v234
	v_and_or_b32 v238, v222, s65, v235
	v_max3_f32 v205, v205, v237, v238
	v_and_or_b32 v237, v214, s66, 6
	v_and_or_b32 v238, v222, s66, 6
	v_max_f32_e32 v174, v174, v237
	v_max_f32_e32 v175, v175, v238
	v_and_or_b32 v237, v215, s65, v234
	v_and_or_b32 v238, v223, s65, v235
	v_max3_f32 v206, v206, v237, v238
	v_and_or_b32 v237, v215, s66, 7
	v_and_or_b32 v238, v223, s66, 7
	v_max_f32_e32 v174, v174, v237
	v_max_f32_e32 v175, v175, v238
	v_or_b32_e32 v237, v173, v174
	v_ashrrev_i32_e32 v238, 31, v174
	v_bitop3_b32 v237, v238, v237, s67 bitop3:0x6c
	ds_max_i32 v236, v237
	v_or_b32_e32 v237, v173, v175
	v_ashrrev_i32_e32 v238, 31, v175
	v_bitop3_b32 v237, v238, v237, s67 bitop3:0x6c
	ds_max_i32 v236, v237 offset:64
	ds_max_i32 v182, v183
	ds_max_i32 v182, v184 offset:64
	v_mov_b32_e32 v0, v161
	v_mov_b32_e32 v1, v160
	v_mov_b32_e32 v3, v162
	v_mov_b32_e32 v4, v163
	v_mov_b32_e32 v5, v203
	v_mov_b32_e32 v6, v204
	v_mov_b32_e32 v7, v205
	v_mov_b32_e32 v8, v206
	s_movk_i32 s2, 0xff80
	s_brev_b32 s3, -2
	v_mbcnt_lo_u32_b32 v2, -1, 0
	s_andn2_b32 s23, s23, 63
	s_lshl_b64 s[0:1], s[16:17], 13
	s_waitcnt vmcnt(0)
	v_mbcnt_hi_u32_b32 v2, -1, v2
	s_add_u32 s4, s10, s0
	v_add_u32_e32 v9, s23, v2
	s_addc_u32 s5, s11, s1
	v_cmp_le_i32_e32 vcc, 0x100, v9
	s_waitcnt lgkmcnt(0)
	s_barrier
	s_and_saveexec_b64 s[0:1], vcc
	s_cbranch_execz .LBB3_35
	v_mov_b32_e32 v10, 0x20000
	v_lshl_add_u32 v10, v9, 2, v10
	ds_read_b32 v10, v10
	s_movk_i32 s6, 0x63
	v_and_b32_e32 v12, 0x7f, v9
	s_waitcnt lgkmcnt(0)
	v_ashrrev_i32_e32 v11, 31, v10
	v_and_b32_e32 v13, 0x7fffffff, v11
	v_bitop3_b32 v11, v11, v10, s3 bitop3:0x6c
	v_lshlrev_b32_e32 v14, 2, v11
	v_and_b32_e32 v14, 16, v14
	s_lshl_b32 s3, s20, 7
	v_bitop3_b32 v13, v13, s6, v10 bitop3:0x48
	v_or3_b32 v13, v13, s3, v14
	v_bfrev_b32_e32 v14, 1
	v_cmp_lt_i32_e32 vcc, -1, v10
	v_lshrrev_b32_e32 v15, 1, v11
	v_and_b32_e32 v15, 12, v15
	v_cndmask_b32_e32 v10, -1, v14, vcc
	v_bitop3_b32 v11, v11, v10, s2 bitop3:0x6c
	s_movk_i32 s2, 0x3ff
	v_bitop3_b32 v10, v13, s2, v15 bitop3:0x36
	s_lshl_b32 s2, s22, 7
	s_addk_i32 s2, 0x80
	v_add_u32_e32 v9, s2, v9
	s_movk_i32 s2, 0x380
	v_and_or_b32 v9, v9, s2, v12
	v_lshlrev_b32_e32 v9, 3, v9
	global_atomic_umax_x2 v9, v[10:11], s[4:5]
